# K1: diag/rows values staged in LDS and written once per workgroup at the end instead of 16-byte stores inside the streaming loop
# baseline (speedup 1.0000x reference)
.Lk1_nozero:
	v_readfirstlane_b32 s15, v66
	s_mov_b32 s18, 0
	s_brev_b32 s19, 1
	v_lshlrev_b32_e32 v69, 4, v62
.LBB0_8:
	s_bitcmp1_b32 s15, 8
	s_cselect_b64 s[20:21], -1, 0
	s_lshr_b32 s16, s15, 2
	s_and_b32 s16, s16, 63
	s_lshl_b64 s[4:5], 1, s16
	s_waitcnt vmcnt(12)
	v_pk_add_f32 v[72:73], v[26:27], v[28:29]
	v_pk_add_f32 v[74:75], v[10:11], v[12:13]
	v_pk_add_f32 v[76:77], v[34:35], v[36:37]
	v_pk_add_f32 v[78:79], v[14:15], v[16:17]
	v_pk_add_f32 v[58:59], v[26:27], v[34:35]
	v_pk_add_f32 v[60:61], v[28:29], v[36:37]
	v_pk_add_f32 v[72:73], v[72:73], v[74:75]
	v_pk_add_f32 v[76:77], v[76:77], v[78:79]
	v_pk_add_f32 v[54:55], v[10:11], v[14:15]
	v_pk_add_f32 v[56:57], v[12:13], v[16:17]
	v_add_f32_e32 v50, v72, v73
	v_add_f32_e32 v51, v76, v77
	s_waitcnt vmcnt(8)
	v_pk_add_f32 v[72:73], v[30:31], v[32:33]
	v_pk_add_f32 v[74:75], v[18:19], v[20:21]
	v_pk_add_f32 v[76:77], v[38:39], v[40:41]
	v_pk_add_f32 v[78:79], v[22:23], v[24:25]
	v_pk_add_f32 v[48:49], v[30:31], v[38:39]
	v_pk_add_f32 v[70:71], v[32:33], v[40:41]
	v_pk_add_f32 v[72:73], v[72:73], v[74:75]
	v_pk_add_f32 v[76:77], v[76:77], v[78:79]
	v_pk_add_f32 v[58:59], v[58:59], v[48:49]
	v_pk_add_f32 v[60:61], v[60:61], v[70:71]
	v_pk_add_f32 v[48:49], v[18:19], v[22:23]
	v_pk_add_f32 v[70:71], v[20:21], v[24:25]
	v_add_f32_e32 v52, v72, v73
	v_add_f32_e32 v53, v76, v77
	v_pk_add_f32 v[2:3], v[2:3], v[58:59]
	v_pk_add_f32 v[4:5], v[4:5], v[60:61]
	v_pk_add_f32 v[54:55], v[54:55], v[48:49]
	v_pk_add_f32 v[56:57], v[56:57], v[70:71]
	v_add_f32_e32 v72, v50, v51
	v_add_f32_e32 v73, v52, v53
	v_pk_add_f32 v[6:7], v[6:7], v[54:55]
	v_pk_add_f32 v[8:9], v[8:9], v[56:57]
	v_add_f32_e32 v72, v72, v73
	v_add_f32_e32 v43, v43, v72
	v_add_f32_dpp v50, v50, v50 quad_perm:[1,0,3,2] row_mask:0xf bank_mask:0xf
	v_add_f32_dpp v51, v51, v51 quad_perm:[1,0,3,2] row_mask:0xf bank_mask:0xf
	v_add_f32_dpp v52, v52, v52 quad_perm:[1,0,3,2] row_mask:0xf bank_mask:0xf
	v_add_f32_dpp v53, v53, v53 quad_perm:[1,0,3,2] row_mask:0xf bank_mask:0xf
	v_add_f32_dpp v50, v50, v50 quad_perm:[2,3,0,1] row_mask:0xf bank_mask:0xf
	v_add_f32_dpp v51, v51, v51 quad_perm:[2,3,0,1] row_mask:0xf bank_mask:0xf
	v_add_f32_dpp v52, v52, v52 quad_perm:[2,3,0,1] row_mask:0xf bank_mask:0xf
	v_add_f32_dpp v53, v53, v53 quad_perm:[2,3,0,1] row_mask:0xf bank_mask:0xf
	v_add_f32_dpp v50, v50, v50 row_half_mirror row_mask:0xf bank_mask:0xf
	v_add_f32_dpp v51, v51, v51 row_half_mirror row_mask:0xf bank_mask:0xf
	v_add_f32_dpp v52, v52, v52 row_half_mirror row_mask:0xf bank_mask:0xf
	v_add_f32_dpp v53, v53, v53 row_half_mirror row_mask:0xf bank_mask:0xf
	v_add_f32_dpp v50, v50, v50 row_mirror row_mask:0xf bank_mask:0xf
	v_add_f32_dpp v51, v51, v51 row_mirror row_mask:0xf bank_mask:0xf
	v_add_f32_dpp v52, v52, v52 row_mirror row_mask:0xf bank_mask:0xf
	v_add_f32_dpp v53, v53, v53 row_mirror row_mask:0xf bank_mask:0xf
	v_add_f32_dpp v50, v50, v50 row_bcast:15 row_mask:0xa bank_mask:0xf
	v_add_f32_dpp v51, v51, v51 row_bcast:15 row_mask:0xa bank_mask:0xf
	v_add_f32_dpp v52, v52, v52 row_bcast:15 row_mask:0xa bank_mask:0xf
	v_add_f32_dpp v53, v53, v53 row_bcast:15 row_mask:0xa bank_mask:0xf
	v_add_f32_dpp v50, v50, v50 row_bcast:31 row_mask:0xc bank_mask:0xf
	v_add_f32_dpp v51, v51, v51 row_bcast:31 row_mask:0xc bank_mask:0xf
	v_add_f32_dpp v52, v52, v52 row_bcast:31 row_mask:0xc bank_mask:0xf
	v_add_f32_dpp v53, v53, v53 row_bcast:31 row_mask:0xc bank_mask:0xf
	s_mov_b64 exec, s[4:5]
	v_cndmask_b32_e64 v58, v26, v10, s[20:21]
	v_cndmask_b32_e64 v59, v35, v15, s[20:21]
	v_cndmask_b32_e64 v60, v32, v20, s[20:21]
	v_cndmask_b32_e64 v61, v41, v25, s[20:21]
	ds_write_b128 v69, v[58:61] offset:8224
	v_add_f32_e32 v72, v58, v59
	v_add_f32_e32 v73, v60, v61
	v_add_f32_e32 v72, v72, v73
	v_add_f32_e32 v42, v42, v72
	s_mov_b64 exec, s[18:19]
	ds_write_b128 v69, v[50:53] offset:8480
	s_mov_b64 exec, -1
	s_add_u32 s15, s15, 16
	v_add_u32_e32 v46, 0x10000, v68
	buffer_load_dwordx4 v[26:29], v46, s[8:11], 0 offen sc0 nt
	buffer_load_dwordx4 v[34:37], v46, s[8:11], 0 offen offset:2048 sc0 nt
	buffer_load_dwordx4 v[10:13], v46, s[8:11], 0 offen offset:1024 sc0 nt
	buffer_load_dwordx4 v[14:17], v46, s[8:11], 0 offen offset:3072 sc0 nt
	v_add_u32_e32 v47, 0x1000, v46
	buffer_load_dwordx4 v[30:33], v47, s[8:11], 0 offen sc0 nt
	buffer_load_dwordx4 v[38:41], v47, s[8:11], 0 offen offset:2048 sc0 nt
	buffer_load_dwordx4 v[18:21], v47, s[8:11], 0 offen offset:1024 sc0 nt
	buffer_load_dwordx4 v[22:25], v47, s[8:11], 0 offen offset:3072 sc0 nt
	s_bitcmp1_b32 s15, 8
	s_cselect_b64 s[20:21], -1, 0
	s_lshr_b32 s16, s15, 2
	s_and_b32 s16, s16, 63
	s_lshl_b64 s[4:5], 1, s16
	s_waitcnt vmcnt(12)
	v_pk_add_f32 v[72:73], v[96:97], v[98:99]
	v_pk_add_f32 v[74:75], v[80:81], v[82:83]
	v_pk_add_f32 v[76:77], v[104:105], v[106:107]
	v_pk_add_f32 v[78:79], v[84:85], v[86:87]
	v_pk_add_f32 v[58:59], v[96:97], v[104:105]
	v_pk_add_f32 v[60:61], v[98:99], v[106:107]
	v_pk_add_f32 v[72:73], v[72:73], v[74:75]
	v_pk_add_f32 v[76:77], v[76:77], v[78:79]
	v_pk_add_f32 v[54:55], v[80:81], v[84:85]
	v_pk_add_f32 v[56:57], v[82:83], v[86:87]
	v_add_f32_e32 v50, v72, v73
	v_add_f32_e32 v51, v76, v77
	s_waitcnt vmcnt(8)
	v_pk_add_f32 v[72:73], v[100:101], v[102:103]
	v_pk_add_f32 v[74:75], v[88:89], v[90:91]
	v_pk_add_f32 v[76:77], v[108:109], v[110:111]
	v_pk_add_f32 v[78:79], v[92:93], v[94:95]
	v_pk_add_f32 v[48:49], v[100:101], v[108:109]
	v_pk_add_f32 v[70:71], v[102:103], v[110:111]
	v_pk_add_f32 v[72:73], v[72:73], v[74:75]
	v_pk_add_f32 v[76:77], v[76:77], v[78:79]
	v_pk_add_f32 v[58:59], v[58:59], v[48:49]
	v_pk_add_f32 v[60:61], v[60:61], v[70:71]
	v_pk_add_f32 v[48:49], v[88:89], v[92:93]
	v_pk_add_f32 v[70:71], v[90:91], v[94:95]
	v_add_f32_e32 v52, v72, v73
	v_add_f32_e32 v53, v76, v77
	v_pk_add_f32 v[2:3], v[2:3], v[58:59]
	v_pk_add_f32 v[4:5], v[4:5], v[60:61]
	v_pk_add_f32 v[54:55], v[54:55], v[48:49]
	v_pk_add_f32 v[56:57], v[56:57], v[70:71]
	v_add_f32_e32 v72, v50, v51
	v_add_f32_e32 v73, v52, v53
	v_pk_add_f32 v[6:7], v[6:7], v[54:55]
	v_pk_add_f32 v[8:9], v[8:9], v[56:57]
	v_add_f32_e32 v72, v72, v73
	v_add_f32_e32 v43, v43, v72
	v_add_f32_dpp v50, v50, v50 quad_perm:[1,0,3,2] row_mask:0xf bank_mask:0xf
	v_add_f32_dpp v51, v51, v51 quad_perm:[1,0,3,2] row_mask:0xf bank_mask:0xf
	v_add_f32_dpp v52, v52, v52 quad_perm:[1,0,3,2] row_mask:0xf bank_mask:0xf
	v_add_f32_dpp v53, v53, v53 quad_perm:[1,0,3,2] row_mask:0xf bank_mask:0xf
	v_add_f32_dpp v50, v50, v50 quad_perm:[2,3,0,1] row_mask:0xf bank_mask:0xf
	v_add_f32_dpp v51, v51, v51 quad_perm:[2,3,0,1] row_mask:0xf bank_mask:0xf
	v_add_f32_dpp v52, v52, v52 quad_perm:[2,3,0,1] row_mask:0xf bank_mask:0xf
	v_add_f32_dpp v53, v53, v53 quad_perm:[2,3,0,1] row_mask:0xf bank_mask:0xf
	v_add_f32_dpp v50, v50, v50 row_half_mirror row_mask:0xf bank_mask:0xf
	v_add_f32_dpp v51, v51, v51 row_half_mirror row_mask:0xf bank_mask:0xf
	v_add_f32_dpp v52, v52, v52 row_half_mirror row_mask:0xf bank_mask:0xf
	v_add_f32_dpp v53, v53, v53 row_half_mirror row_mask:0xf bank_mask:0xf
	v_add_f32_dpp v50, v50, v50 row_mirror row_mask:0xf bank_mask:0xf
	v_add_f32_dpp v51, v51, v51 row_mirror row_mask:0xf bank_mask:0xf
	v_add_f32_dpp v52, v52, v52 row_mirror row_mask:0xf bank_mask:0xf
	v_add_f32_dpp v53, v53, v53 row_mirror row_mask:0xf bank_mask:0xf
	v_add_f32_dpp v50, v50, v50 row_bcast:15 row_mask:0xa bank_mask:0xf
	v_add_f32_dpp v51, v51, v51 row_bcast:15 row_mask:0xa bank_mask:0xf
	v_add_f32_dpp v52, v52, v52 row_bcast:15 row_mask:0xa bank_mask:0xf
	v_add_f32_dpp v53, v53, v53 row_bcast:15 row_mask:0xa bank_mask:0xf
	v_add_f32_dpp v50, v50, v50 row_bcast:31 row_mask:0xc bank_mask:0xf
	v_add_f32_dpp v51, v51, v51 row_bcast:31 row_mask:0xc bank_mask:0xf
	v_add_f32_dpp v52, v52, v52 row_bcast:31 row_mask:0xc bank_mask:0xf
	v_add_f32_dpp v53, v53, v53 row_bcast:31 row_mask:0xc bank_mask:0xf
	s_mov_b64 exec, s[4:5]
	v_cndmask_b32_e64 v58, v96, v80, s[20:21]
	v_cndmask_b32_e64 v59, v105, v85, s[20:21]
	v_cndmask_b32_e64 v60, v102, v90, s[20:21]
	v_cndmask_b32_e64 v61, v111, v95, s[20:21]
	ds_write_b128 v69, v[58:61] offset:8288
	v_add_f32_e32 v72, v58, v59
	v_add_f32_e32 v73, v60, v61
	v_add_f32_e32 v72, v72, v73
	v_add_f32_e32 v42, v42, v72
	s_mov_b64 exec, s[18:19]
	ds_write_b128 v69, v[50:53] offset:8544
	s_mov_b64 exec, -1
	s_add_u32 s15, s15, 16
	v_add_u32_e32 v46, 0x18000, v68
	buffer_load_dwordx4 v[96:99], v46, s[8:11], 0 offen sc0 nt
	buffer_load_dwordx4 v[104:107], v46, s[8:11], 0 offen offset:2048 sc0 nt
	buffer_load_dwordx4 v[80:83], v46, s[8:11], 0 offen offset:1024 sc0 nt
	buffer_load_dwordx4 v[84:87], v46, s[8:11], 0 offen offset:3072 sc0 nt
	v_add_u32_e32 v47, 0x1000, v46
	buffer_load_dwordx4 v[100:103], v47, s[8:11], 0 offen sc0 nt
	buffer_load_dwordx4 v[108:111], v47, s[8:11], 0 offen offset:2048 sc0 nt
	buffer_load_dwordx4 v[88:91], v47, s[8:11], 0 offen offset:1024 sc0 nt
	buffer_load_dwordx4 v[92:95], v47, s[8:11], 0 offen offset:3072 sc0 nt
	s_bitcmp1_b32 s15, 8
	s_cselect_b64 s[20:21], -1, 0
	s_lshr_b32 s16, s15, 2
	s_and_b32 s16, s16, 63
	s_lshl_b64 s[4:5], 1, s16
	s_waitcnt vmcnt(12)
	v_pk_add_f32 v[72:73], v[26:27], v[28:29]
	v_pk_add_f32 v[74:75], v[10:11], v[12:13]
	v_pk_add_f32 v[76:77], v[34:35], v[36:37]
	v_pk_add_f32 v[78:79], v[14:15], v[16:17]
	v_pk_add_f32 v[58:59], v[26:27], v[34:35]
	v_pk_add_f32 v[60:61], v[28:29], v[36:37]
	v_pk_add_f32 v[72:73], v[72:73], v[74:75]
	v_pk_add_f32 v[76:77], v[76:77], v[78:79]
	v_pk_add_f32 v[54:55], v[10:11], v[14:15]
	v_pk_add_f32 v[56:57], v[12:13], v[16:17]
	v_add_f32_e32 v50, v72, v73
	v_add_f32_e32 v51, v76, v77
	s_waitcnt vmcnt(8)
	v_pk_add_f32 v[72:73], v[30:31], v[32:33]
	v_pk_add_f32 v[74:75], v[18:19], v[20:21]
	v_pk_add_f32 v[76:77], v[38:39], v[40:41]
	v_pk_add_f32 v[78:79], v[22:23], v[24:25]
	v_pk_add_f32 v[48:49], v[30:31], v[38:39]
	v_pk_add_f32 v[70:71], v[32:33], v[40:41]
	v_pk_add_f32 v[72:73], v[72:73], v[74:75]
	v_pk_add_f32 v[76:77], v[76:77], v[78:79]
	v_pk_add_f32 v[58:59], v[58:59], v[48:49]
	v_pk_add_f32 v[60:61], v[60:61], v[70:71]
	v_pk_add_f32 v[48:49], v[18:19], v[22:23]
	v_pk_add_f32 v[70:71], v[20:21], v[24:25]
	v_add_f32_e32 v52, v72, v73
	v_add_f32_e32 v53, v76, v77
	v_pk_add_f32 v[2:3], v[2:3], v[58:59]
	v_pk_add_f32 v[4:5], v[4:5], v[60:61]
	v_pk_add_f32 v[54:55], v[54:55], v[48:49]
	v_pk_add_f32 v[56:57], v[56:57], v[70:71]
	v_add_f32_e32 v72, v50, v51
	v_add_f32_e32 v73, v52, v53
	v_pk_add_f32 v[6:7], v[6:7], v[54:55]
	v_pk_add_f32 v[8:9], v[8:9], v[56:57]
	v_add_f32_e32 v72, v72, v73
	v_add_f32_e32 v43, v43, v72
	v_add_f32_dpp v50, v50, v50 quad_perm:[1,0,3,2] row_mask:0xf bank_mask:0xf
	v_add_f32_dpp v51, v51, v51 quad_perm:[1,0,3,2] row_mask:0xf bank_mask:0xf
	v_add_f32_dpp v52, v52, v52 quad_perm:[1,0,3,2] row_mask:0xf bank_mask:0xf
	v_add_f32_dpp v53, v53, v53 quad_perm:[1,0,3,2] row_mask:0xf bank_mask:0xf
	v_add_f32_dpp v50, v50, v50 quad_perm:[2,3,0,1] row_mask:0xf bank_mask:0xf
	v_add_f32_dpp v51, v51, v51 quad_perm:[2,3,0,1] row_mask:0xf bank_mask:0xf
	v_add_f32_dpp v52, v52, v52 quad_perm:[2,3,0,1] row_mask:0xf bank_mask:0xf
	v_add_f32_dpp v53, v53, v53 quad_perm:[2,3,0,1] row_mask:0xf bank_mask:0xf
	v_add_f32_dpp v50, v50, v50 row_half_mirror row_mask:0xf bank_mask:0xf
	v_add_f32_dpp v51, v51, v51 row_half_mirror row_mask:0xf bank_mask:0xf
	v_add_f32_dpp v52, v52, v52 row_half_mirror row_mask:0xf bank_mask:0xf
	v_add_f32_dpp v53, v53, v53 row_half_mirror row_mask:0xf bank_mask:0xf
	v_add_f32_dpp v50, v50, v50 row_mirror row_mask:0xf bank_mask:0xf
	v_add_f32_dpp v51, v51, v51 row_mirror row_mask:0xf bank_mask:0xf
	v_add_f32_dpp v52, v52, v52 row_mirror row_mask:0xf bank_mask:0xf
	v_add_f32_dpp v53, v53, v53 row_mirror row_mask:0xf bank_mask:0xf
	v_add_f32_dpp v50, v50, v50 row_bcast:15 row_mask:0xa bank_mask:0xf
	v_add_f32_dpp v51, v51, v51 row_bcast:15 row_mask:0xa bank_mask:0xf
	v_add_f32_dpp v52, v52, v52 row_bcast:15 row_mask:0xa bank_mask:0xf
	v_add_f32_dpp v53, v53, v53 row_bcast:15 row_mask:0xa bank_mask:0xf
	v_add_f32_dpp v50, v50, v50 row_bcast:31 row_mask:0xc bank_mask:0xf
	v_add_f32_dpp v51, v51, v51 row_bcast:31 row_mask:0xc bank_mask:0xf
	v_add_f32_dpp v52, v52, v52 row_bcast:31 row_mask:0xc bank_mask:0xf
	v_add_f32_dpp v53, v53, v53 row_bcast:31 row_mask:0xc bank_mask:0xf
	s_mov_b64 exec, s[4:5]
	v_cndmask_b32_e64 v58, v26, v10, s[20:21]
	v_cndmask_b32_e64 v59, v35, v15, s[20:21]
	v_cndmask_b32_e64 v60, v32, v20, s[20:21]
	v_cndmask_b32_e64 v61, v41, v25, s[20:21]
	ds_write_b128 v69, v[58:61] offset:8352
	v_add_f32_e32 v72, v58, v59
	v_add_f32_e32 v73, v60, v61
	v_add_f32_e32 v72, v72, v73
	v_add_f32_e32 v42, v42, v72
	s_mov_b64 exec, s[18:19]
	ds_write_b128 v69, v[50:53] offset:8608
	s_mov_b64 exec, -1
	s_add_u32 s15, s15, 16
	s_bitcmp1_b32 s15, 8
	s_cselect_b64 s[20:21], -1, 0
	s_lshr_b32 s16, s15, 2
	s_and_b32 s16, s16, 63
	s_lshl_b64 s[4:5], 1, s16
	s_waitcnt vmcnt(4)
	v_pk_add_f32 v[72:73], v[96:97], v[98:99]
	v_pk_add_f32 v[74:75], v[80:81], v[82:83]
	v_pk_add_f32 v[76:77], v[104:105], v[106:107]
	v_pk_add_f32 v[78:79], v[84:85], v[86:87]
	v_pk_add_f32 v[58:59], v[96:97], v[104:105]
	v_pk_add_f32 v[60:61], v[98:99], v[106:107]
	v_pk_add_f32 v[72:73], v[72:73], v[74:75]
	v_pk_add_f32 v[76:77], v[76:77], v[78:79]
	v_pk_add_f32 v[54:55], v[80:81], v[84:85]
	v_pk_add_f32 v[56:57], v[82:83], v[86:87]
	v_add_f32_e32 v50, v72, v73
	v_add_f32_e32 v51, v76, v77
	s_waitcnt vmcnt(0)
	v_pk_add_f32 v[72:73], v[100:101], v[102:103]
	v_pk_add_f32 v[74:75], v[88:89], v[90:91]
	v_pk_add_f32 v[76:77], v[108:109], v[110:111]
	v_pk_add_f32 v[78:79], v[92:93], v[94:95]
	v_pk_add_f32 v[48:49], v[100:101], v[108:109]
	v_pk_add_f32 v[70:71], v[102:103], v[110:111]
	v_pk_add_f32 v[72:73], v[72:73], v[74:75]
	v_pk_add_f32 v[76:77], v[76:77], v[78:79]
	v_pk_add_f32 v[58:59], v[58:59], v[48:49]
	v_pk_add_f32 v[60:61], v[60:61], v[70:71]
	v_pk_add_f32 v[48:49], v[88:89], v[92:93]
	v_pk_add_f32 v[70:71], v[90:91], v[94:95]
	v_add_f32_e32 v52, v72, v73
	v_add_f32_e32 v53, v76, v77
	v_pk_add_f32 v[2:3], v[2:3], v[58:59]
	v_pk_add_f32 v[4:5], v[4:5], v[60:61]
	v_pk_add_f32 v[54:55], v[54:55], v[48:49]
	v_pk_add_f32 v[56:57], v[56:57], v[70:71]
	v_add_f32_e32 v72, v50, v51
	v_add_f32_e32 v73, v52, v53
	v_pk_add_f32 v[6:7], v[6:7], v[54:55]
	v_pk_add_f32 v[8:9], v[8:9], v[56:57]
	v_add_f32_e32 v72, v72, v73
	v_add_f32_e32 v43, v43, v72
	v_add_f32_dpp v50, v50, v50 quad_perm:[1,0,3,2] row_mask:0xf bank_mask:0xf
	v_add_f32_dpp v51, v51, v51 quad_perm:[1,0,3,2] row_mask:0xf bank_mask:0xf
	v_add_f32_dpp v52, v52, v52 quad_perm:[1,0,3,2] row_mask:0xf bank_mask:0xf
	v_add_f32_dpp v53, v53, v53 quad_perm:[1,0,3,2] row_mask:0xf bank_mask:0xf
	v_add_f32_dpp v50, v50, v50 quad_perm:[2,3,0,1] row_mask:0xf bank_mask:0xf
	v_add_f32_dpp v51, v51, v51 quad_perm:[2,3,0,1] row_mask:0xf bank_mask:0xf
	v_add_f32_dpp v52, v52, v52 quad_perm:[2,3,0,1] row_mask:0xf bank_mask:0xf
	v_add_f32_dpp v53, v53, v53 quad_perm:[2,3,0,1] row_mask:0xf bank_mask:0xf
	v_add_f32_dpp v50, v50, v50 row_half_mirror row_mask:0xf bank_mask:0xf
	v_add_f32_dpp v51, v51, v51 row_half_mirror row_mask:0xf bank_mask:0xf
	v_add_f32_dpp v52, v52, v52 row_half_mirror row_mask:0xf bank_mask:0xf
	v_add_f32_dpp v53, v53, v53 row_half_mirror row_mask:0xf bank_mask:0xf
	v_add_f32_dpp v50, v50, v50 row_mirror row_mask:0xf bank_mask:0xf
	v_add_f32_dpp v51, v51, v51 row_mirror row_mask:0xf bank_mask:0xf
	v_add_f32_dpp v52, v52, v52 row_mirror row_mask:0xf bank_mask:0xf
	v_add_f32_dpp v53, v53, v53 row_mirror row_mask:0xf bank_mask:0xf
	v_add_f32_dpp v50, v50, v50 row_bcast:15 row_mask:0xa bank_mask:0xf
	v_add_f32_dpp v51, v51, v51 row_bcast:15 row_mask:0xa bank_mask:0xf
	v_add_f32_dpp v52, v52, v52 row_bcast:15 row_mask:0xa bank_mask:0xf
	v_add_f32_dpp v53, v53, v53 row_bcast:15 row_mask:0xa bank_mask:0xf
	v_add_f32_dpp v50, v50, v50 row_bcast:31 row_mask:0xc bank_mask:0xf
	v_add_f32_dpp v51, v51, v51 row_bcast:31 row_mask:0xc bank_mask:0xf
	v_add_f32_dpp v52, v52, v52 row_bcast:31 row_mask:0xc bank_mask:0xf
	v_add_f32_dpp v53, v53, v53 row_bcast:31 row_mask:0xc bank_mask:0xf
	s_mov_b64 exec, s[4:5]
	v_cndmask_b32_e64 v58, v96, v80, s[20:21]
	v_cndmask_b32_e64 v59, v105, v85, s[20:21]
	v_cndmask_b32_e64 v60, v102, v90, s[20:21]
	v_cndmask_b32_e64 v61, v111, v95, s[20:21]
	ds_write_b128 v69, v[58:61] offset:8416
	v_add_f32_e32 v72, v58, v59
	v_add_f32_e32 v73, v60, v61
	v_add_f32_e32 v72, v72, v73
	v_add_f32_e32 v42, v42, v72
	s_mov_b64 exec, s[18:19]
	ds_write_b128 v69, v[50:53] offset:8672
	s_mov_b64 exec, -1
	s_add_u32 s15, s15, 16

.LBB0_25:
	v_subrev_u32_e32 v10, 0xc0, v0
	v_cmp_gt_u32_e32 vcc, 32, v10
	s_and_saveexec_b64 s[8:9], vcc
	s_cbranch_execz .Lk1_nodr
	v_lshlrev_b32_e32 v11, 4, v10
	ds_read_b128 v[12:15], v11 offset:8224
	v_and_b32_e32 v16, 15, v10
	v_lshlrev_b32_e32 v16, 4, v16
	v_lshrrev_b32_e32 v17, 4, v10
	v_lshl_add_u32 v16, v17, 18, v16
	s_lshl_b32 s10, s2, 8
	v_add_u32_e32 v16, s10, v16
	s_waitcnt lgkmcnt(0)
	global_store_dwordx4 v16, v[12:15], s[6:7]
.Lk1_nodr:
	s_or_b64 exec, exec, s[8:9]
	s_movk_i32 s4, 0x80
	v_cmp_eq_u32_e32 vcc, s4, v0
	s_and_saveexec_b64 s[4:5], vcc
	s_cbranch_execz .LBB0_27
	v_mov_b32_e32 v8, 0
	ds_read_b128 v[0:3], v8 offset:8192
	ds_read_b128 v[4:7], v8 offset:8208
	s_and_b32 s8, s2, -8
	s_or_b32 s3, s8, s3
	s_add_i32 s8, s3, 0xa0000
	s_mov_b32 s9, 0
	s_lshl_b64 s[10:11], s[8:9], 2
	s_add_u32 s10, s6, s10
	s_waitcnt lgkmcnt(1)
	v_add_f32_e32 v0, v0, v2
	s_waitcnt lgkmcnt(0)
	v_add_f32_e32 v2, v4, v6
	s_addc_u32 s11, s7, s11
	s_add_i32 s8, s3, 0xa0400
	v_add_f32_e32 v0, v0, v2
	s_lshl_b64 s[8:9], s[8:9], 2
	global_store_dword v8, v0, s[10:11]
	v_add_f32_e32 v0, v1, v3
	v_add_f32_e32 v1, v5, v7
	s_add_u32 s8, s6, s8
	v_add_f32_e32 v0, v0, v1
	s_addc_u32 s9, s7, s9
	global_store_dword v8, v0, s[8:9]

	.amdhsa_kernel _Z9k1_streamPKfPf6PfArgs
		.amdhsa_group_segment_fixed_size 8736
		.amdhsa_private_segment_fixed_size 0
		.amdhsa_kernarg_size 80
		.amdhsa_user_sgpr_count 2
		.amdhsa_user_sgpr_dispatch_ptr 0
		.amdhsa_user_sgpr_queue_ptr 0
		.amdhsa_user_sgpr_kernarg_segment_ptr 1
		.amdhsa_user_sgpr_dispatch_id 0
		.amdhsa_user_sgpr_kernarg_preload_length 0
		.amdhsa_user_sgpr_kernarg_preload_offset 0
		.amdhsa_user_sgpr_private_segment_size 0
		.amdhsa_uses_dynamic_stack 0
		.amdhsa_enable_private_segment 0
		.amdhsa_system_sgpr_workgroup_id_x 1
		.amdhsa_system_sgpr_workgroup_id_y 0
		.amdhsa_system_sgpr_workgroup_id_z 0
		.amdhsa_system_sgpr_workgroup_info 0
		.amdhsa_system_vgpr_workitem_id 0
		.amdhsa_next_free_vgpr 112
		.amdhsa_next_free_sgpr 22
		.amdhsa_accum_offset 112
		.amdhsa_reserve_vcc 1
		.amdhsa_float_round_mode_32 0
		.amdhsa_float_round_mode_16_64 0
		.amdhsa_float_denorm_mode_32 3
		.amdhsa_float_denorm_mode_16_64 3
		.amdhsa_dx10_clamp 1
		.amdhsa_ieee_mode 1
		.amdhsa_fp16_overflow 0
		.amdhsa_tg_split 0
		.amdhsa_exception_fp_ieee_invalid_op 0
		.amdhsa_exception_fp_denorm_src 0
		.amdhsa_exception_fp_ieee_div_zero 0
		.amdhsa_exception_fp_ieee_overflow 0
		.amdhsa_exception_fp_ieee_underflow 0
		.amdhsa_exception_fp_ieee_inexact 0
		.amdhsa_exception_int_div_zero 0
	.end_amdhsa_kernel

amdhsa.kernels:
  - .agpr_count:     0
    .args:
      - .actual_access:  read_only
        .address_space:  global
        .offset:         0
        .size:           8
        .value_kind:     global_buffer
      - .actual_access:  write_only
        .address_space:  global
        .offset:         8
        .size:           8
        .value_kind:     global_buffer
      - .offset:         16
        .size:           64
        .value_kind:     by_value
    .group_segment_fixed_size: 8736
    .kernarg_segment_align: 8
    .kernarg_segment_size: 80
    .language:       OpenCL C
    .language_version:
      - 2
      - 0
    .max_flat_workgroup_size: 256
    .name:           _Z9k1_streamPKfPf6PfArgs
    .private_segment_fixed_size: 0
    .sgpr_count:     28
    .sgpr_spill_count: 0
    .symbol:         _Z9k1_streamPKfPf6PfArgs.kd
    .uniform_work_group_size: 1
    .uses_dynamic_stack: false
    .vgpr_count:     112
    .vgpr_spill_count: 0
    .wavefront_size: 64
  - .agpr_count:     0
    .args:
      - .actual_access:  read_only
        .address_space:  global
        .offset:         0
        .size:           8
        .value_kind:     global_buffer
      - .actual_access:  read_only
        .address_space:  global
        .offset:         8
        .size:           8
        .value_kind:     global_buffer
      - .actual_access:  read_only
        .address_space:  global
        .offset:         16
        .size:           8
        .value_kind:     global_buffer
      - .actual_access:  write_only
        .address_space:  global
        .offset:         24
        .size:           8
        .value_kind:     global_buffer
      - .address_space:  global
        .offset:         32
        .size:           8
        .value_kind:     global_buffer
      - .address_space:  global
        .offset:         40
        .size:           8
        .value_kind:     global_buffer
    .group_segment_fixed_size: 3712
    .kernarg_segment_align: 8
    .kernarg_segment_size: 48
    .language:       OpenCL C
    .language_version:
      - 2
      - 0
    .max_flat_workgroup_size: 256
    .name:           _Z9k2_layer1PKfS0_S0_PfS1_S1_
    .private_segment_fixed_size: 0
    .sgpr_count:     32
    .sgpr_spill_count: 0
    .symbol:         _Z9k2_layer1PKfS0_S0_PfS1_S1_.kd
    .uniform_work_group_size: 1
    .uses_dynamic_stack: false
    .vgpr_count:     92
    .vgpr_spill_count: 0
    .wavefront_size: 64
  - .agpr_count:     8
    .args:
      - .actual_access:  read_only
        .address_space:  global
        .offset:         0
        .size:           8
        .value_kind:     global_buffer
      - .actual_access:  read_only
        .address_space:  global
        .offset:         8
        .size:           8
        .value_kind:     global_buffer
      - .actual_access:  read_only
        .address_space:  global
        .offset:         16
        .size:           8
        .value_kind:     global_buffer
      - .actual_access:  read_only
        .address_space:  global
        .offset:         24
        .size:           8
        .value_kind:     global_buffer
      - .actual_access:  read_only
        .address_space:  global
        .offset:         32
        .size:           8
        .value_kind:     global_buffer
      - .actual_access:  read_only
        .address_space:  global
        .offset:         40
        .size:           8
        .value_kind:     global_buffer
      - .actual_access:  read_only
        .address_space:  global
        .offset:         48
        .size:           8
        .value_kind:     global_buffer
      - .actual_access:  write_only
        .address_space:  global
        .offset:         56
        .size:           8
        .value_kind:     global_buffer
      - .address_space:  global
        .offset:         64
        .size:           8
        .value_kind:     global_buffer
      - .address_space:  global
        .offset:         72
        .size:           8
        .value_kind:     global_buffer
    .group_segment_fixed_size: 1280
    .kernarg_segment_align: 8
    .kernarg_segment_size: 80
    .language:       OpenCL C
    .language_version:
      - 2
      - 0
    .max_flat_workgroup_size: 256
    .name:           _Z7k_layerPKfS0_S0_S0_S0_S0_S0_PfS1_S1_
    .private_segment_fixed_size: 0
    .sgpr_count:     40
    .sgpr_spill_count: 0
    .symbol:         _Z7k_layerPKfS0_S0_S0_S0_S0_S0_PfS1_S1_.kd
    .uniform_work_group_size: 1
    .uses_dynamic_stack: false
    .vgpr_count:     104
    .vgpr_spill_count: 0
    .wavefront_size: 64
  - .agpr_count:     12
    .args:
      - .actual_access:  read_only
        .address_space:  global
        .offset:         0
        .size:           8
        .value_kind:     global_buffer
      - .actual_access:  read_only
        .address_space:  global
        .offset:         8
        .size:           8
        .value_kind:     global_buffer
      - .actual_access:  read_only
        .address_space:  global
        .offset:         16
        .size:           8
        .value_kind:     global_buffer
      - .actual_access:  read_only
        .address_space:  global
        .offset:         24
        .size:           8
        .value_kind:     global_buffer
      - .actual_access:  read_only
        .address_space:  global
        .offset:         32
        .size:           8
        .value_kind:     global_buffer
      - .actual_access:  read_only
        .address_space:  global
        .offset:         40
        .size:           8
        .value_kind:     global_buffer
      - .actual_access:  read_only
        .address_space:  global
        .offset:         48
        .size:           8
        .value_kind:     global_buffer
      - .actual_access:  read_only
        .address_space:  global
        .offset:         56
        .size:           8
        .value_kind:     global_buffer
      - .actual_access:  read_only
        .address_space:  global
        .offset:         64
        .size:           8
        .value_kind:     global_buffer
      - .actual_access:  write_only
        .address_space:  global
        .offset:         72
        .size:           8
        .value_kind:     global_buffer
    .group_segment_fixed_size: 4608
    .kernarg_segment_align: 8
    .kernarg_segment_size: 80
    .language:       OpenCL C
    .language_version:
      - 2
      - 0
    .max_flat_workgroup_size: 256
    .name:           _Z8k5_finalPKfS0_S0_S0_S0_S0_S0_S0_S0_Pf
    .private_segment_fixed_size: 0
    .sgpr_count:     30
    .sgpr_spill_count: 0
    .symbol:         _Z8k5_finalPKfS0_S0_S0_S0_S0_S0_S0_S0_Pf.kd
    .uniform_work_group_size: 1
    .uses_dynamic_stack: false
    .vgpr_count:     96
    .vgpr_spill_count: 0
    .wavefront_size: 64
